# attention: static s_setprio 1 for waves 4-7 during the attention unit loop (on top of gates epilogue rewrite)
# speedup vs baseline: 1.0071x; 1.0071x over previous
; #define LAS __attribute__((address_space(3)))
; __device__ __forceinline__ unsigned f2bf(float f) { unsigned u = __builtin_bit_cast(unsigned, f); return (u + 0x7fffu + ((u >> 16) & 1u)) >> 16; }
; __device__ __forceinline__ int crow(int r, int hi) { return (r & 3) + 8 * (r >> 2) + 4 * hi; }
; #define PHASE_BEGIN() Ctx c = c0; { int t_ = c0.tid; asm volatile("" : "+v"(t_)); c.tid = t_; c.lane = t_ & 63; c.wave = __builtin_amdgcn_readfirstlane(t_ >> 6); } \
;     GAS unsigned char* wsb = (GAS unsigned char*)a.ws; asm volatile("" : "+s"(wsb));
; __device__ __forceinline__ void attn_unit(const bf16* __restrict__ Qraw, const float* __restrict__ ssq, const float* __restrict__ qn, int t0, const bf16* __restrict__ Kh, const bf16* __restrict__ Vh, bf16* __restrict__ Ob, int seq, LAS char* lds, int tid) {
;     ...
;     if (hi == 0) li_l[r32] = l_reg; asm volatile("s_waitcnt lgkmcnt(0)" ::: "memory");
;     float rli[16];
; #pragma unroll
;     for (int r = 0; r < 16; ++r) rli[r] = __builtin_amdgcn_rcpf(li_l[crow(r, hi)]);
;     char* Ow = (char*)Ob + (size_t)(wid * QBLK) * DM * 2; const unsigned ooff = (unsigned)(4 * hi * DM + r32) * 2u;
; #pragma unroll
;     for (int r = 0; r < 16; ++r) {
; #pragma unroll
;         for (int d0 = 0; d0 < 4; ++d0) *(bf16*)(Ow + (((r & 3) + 8 * (r >> 2)) * DM + d0 * 32) * 2 + ooff) = (bf16)f2bf(o[d0][r] * rli[r]); }
; __device__ __forceinline__ void phase_attn(const Args& a, const Ctx& c0, int l, bool last) {
;     PHASE_BEGIN();
;     const bf16* QRAW = WSP(const bf16, WS_QRAW); const float* SSQ = WSP(const float, WS_SSQ); const bf16* K = WSP(const bf16, WS_K); const bf16* V = WSP(const bf16, WS_V); bf16* Y = WSP(bf16, WS_Y);
;     const float* qn = INP(19) + (size_t)l * DQK;
;     const int nun = last ? 512 : 544;
;     for (int rep = 0; rep < NREP(13); ++rep)
;     for (int u = c.bid; u < nun; u += c.G) {
;         const bool isl = u < 512; const int bh = isl ? (u >> 4) : (u - 512), qb = u & 15, b = bh >> 3, h = bh & 7;
;         const int grow0 = isl ? b * SEQ + qb * 256 : NL + b * CTXL;
;         int tu = c0.tid; asm volatile("" : "+v"(tu));
;         att::attn_unit(QRAW + (size_t)grow0 * 1536 + h * DQK, SSQ + (size_t)grow0 * 16, qn, isl ? qb * 256 : -1, K + (size_t)bh * KVLEN * DQK, V + (size_t)bh * KVLEN * DVH,
;                        Y + (size_t)grow0 * DM + RW + h * DVH, isl ? KVLEN : CTXL, (LAS char*)c.lds, tu);
.LBB0_1445:
	v_readlane_b32 s2, v254, 11
	v_readlane_b32 s3, v254, 12
	s_and_b64 s[2:3], s[2:3], exec
	s_movk_i32 s2, 0x200
	v_readlane_b32 s4, v254, 21
	s_cselect_b32 s44, s2, 0x220
	v_readlane_b32 s6, v254, 23
	v_readlane_b32 s7, v254, 24
	s_cmp_ge_i32 s90, s44
	v_mov_b32_e32 v2, v0
	s_mov_b64 s[2:3], s[6:7]
	v_readlane_b32 s5, v254, 22
	s_cbranch_scc1 .LBB0_1483
	v_readlane_b32 s4, v254, 17
	v_readlane_b32 s5, v254, 18
	s_mul_i32 s12, s4, 0xc0
	v_readlane_b32 s48, v254, 35
	s_lshl_b64 s[4:5], s[12:13], 2
	v_readlane_b32 s56, v254, 43
	v_readlane_b32 s57, v254, 44
	s_add_u32 s4, s56, s4
	s_addc_u32 s5, s57, s5
	s_add_u32 s45, s2, 0x63e00000
	s_addc_u32 s46, s3, 0
	s_add_u32 s47, s2, 0x67100000
	v_readlane_b32 s49, v254, 36
	s_addc_u32 s48, s3, 0
	v_readlane_b32 s50, v254, 37
	s_add_u32 s49, s2, 0x43200000
	v_readlane_b32 s51, v254, 38
	s_addc_u32 s50, s3, 0
	v_readlane_b32 s52, v254, 39
	s_add_u32 s51, s2, 0x46500000
	v_readlane_b32 s53, v254, 40
	s_addc_u32 s52, s3, 0
	v_readlane_b32 s54, v254, 41
	v_readlane_b32 s55, v254, 42
	s_add_u32 s53, s2, 0x48700000
	s_addc_u32 s54, s3, 0
	s_mov_b32 s55, s90
	v_readlane_b32 s58, v254, 45
	v_readlane_b32 s59, v254, 46
	v_readlane_b32 s60, v254, 47
	v_readlane_b32 s61, v254, 48
	v_readlane_b32 s62, v254, 49
	v_readlane_b32 s63, v254, 50
	v_readfirstlane_b32 s6, v0
	s_nop 3
	s_cmpk_lt_u32 s6, 0x100
	s_cbranch_scc1 .Lattn_prio_skip
	s_setprio 1
.Lattn_prio_skip:
	s_branch .LBB0_1448
.LBB0_1447:
	s_or_b64 exec, exec, s[10:11]
	s_waitcnt lgkmcnt(0)
	v_add_u32_e32 v1, s58, v188
	ds_read_b128 v[66:69], v1
	ds_read_b128 v[70:73], v1 offset:32
	s_lshl_b64 s[6:7], s[6:7], 12
	s_add_u32 s6, s53, s6
	s_addc_u32 s7, s54, s7
	s_waitcnt lgkmcnt(1)
	v_rcp_f32_e32 v74, v66
	v_rcp_f32_e32 v75, v67
	v_rcp_f32_e32 v76, v68
	v_rcp_f32_e32 v77, v69
	ds_read_b128 v[66:69], v1 offset:64
	s_lshl_b32 s10, s56, 8
	s_add_u32 s10, s6, s10
	s_addc_u32 s11, s7, 0
	s_lshl_b64 s[6:7], s[8:9], 12
	v_mul_f32_e32 v2, v2, v74
	s_waitcnt lgkmcnt(1)
	v_rcp_f32_e32 v78, v70
	v_rcp_f32_e32 v79, v71
	v_rcp_f32_e32 v80, v72
	v_rcp_f32_e32 v81, v73
	ds_read_b128 v[70:73], v1 offset:96
	s_waitcnt lgkmcnt(1)
	v_rcp_f32_e32 v1, v66
	s_add_u32 s6, s10, s6
	v_lshlrev_b32_e32 v66, 1, v186
	v_bfe_u32 v83, v2, 16, 1
	s_addc_u32 s7, s11, s7
	v_lshl_or_b32 v146, v187, 14, v66
	v_add3_u32 v2, v2, v83, s37
	global_store_short_d16_hi v146, v2, s[6:7] offset:2048
	v_mul_f32_e32 v2, v50, v74
	v_bfe_u32 v50, v2, 16, 1
	v_add3_u32 v2, v2, v50, s37
	global_store_short_d16_hi v146, v2, s[6:7] offset:2112
	v_mul_f32_e32 v2, v34, v74
	v_bfe_u32 v34, v2, 16, 1
	v_add3_u32 v2, v2, v34, s37
	global_store_short_d16_hi v146, v2, s[6:7] offset:2176
	v_mul_f32_e32 v2, v18, v74
	v_bfe_u32 v18, v2, 16, 1
	v_add3_u32 v2, v2, v18, s37
	global_store_short_d16_hi v146, v2, s[6:7] offset:2240
	v_mul_f32_e32 v2, v3, v75
	v_rcp_f32_e32 v82, v67
	v_lshl_add_u64 v[66:67], s[6:7], 0, v[146:147]
	v_bfe_u32 v3, v2, 16, 1
	v_add3_u32 v18, v2, v3, s37
	v_add_co_u32_e32 v2, vcc, s87, v66
	s_movk_i32 s6, 0x3000
	s_nop 0
	v_addc_co_u32_e32 v3, vcc, 0, v67, vcc
	global_store_short_d16_hi v[2:3], v18, off offset:2048
	v_mul_f32_e32 v18, v51, v75
	v_bfe_u32 v34, v18, 16, 1
	v_add3_u32 v18, v18, v34, s37
	global_store_short_d16_hi v[2:3], v18, off offset:2112
	v_mul_f32_e32 v18, v35, v75
	v_bfe_u32 v34, v18, 16, 1
	v_add3_u32 v18, v18, v34, s37
	global_store_short_d16_hi v[2:3], v18, off offset:2176
	v_mul_f32_e32 v18, v19, v75
	v_bfe_u32 v19, v18, 16, 1
	v_add3_u32 v18, v18, v19, s37
	global_store_short_d16_hi v[2:3], v18, off offset:2240
	v_mul_f32_e32 v2, v4, v76
	v_bfe_u32 v3, v2, 16, 1
	v_add3_u32 v4, v2, v3, s37
	v_add_co_u32_e32 v2, vcc, s80, v66
	v_rcp_f32_e32 v68, v68
	s_nop 0
	v_addc_co_u32_e32 v3, vcc, 0, v67, vcc
	global_store_short_d16_hi v[2:3], v4, off offset:2048
	v_mul_f32_e32 v4, v52, v76
	v_bfe_u32 v18, v4, 16, 1
	v_add3_u32 v4, v4, v18, s37
	global_store_short_d16_hi v[2:3], v4, off offset:2112
	v_mul_f32_e32 v4, v36, v76
	v_bfe_u32 v18, v4, 16, 1
	v_add3_u32 v4, v4, v18, s37
	global_store_short_d16_hi v[2:3], v4, off offset:2176
	v_mul_f32_e32 v4, v20, v76
	v_bfe_u32 v18, v4, 16, 1
	v_add3_u32 v4, v4, v18, s37
	global_store_short_d16_hi v[2:3], v4, off offset:2240
	v_mul_f32_e32 v2, v5, v77
	v_bfe_u32 v3, v2, 16, 1
	v_add3_u32 v4, v2, v3, s37
	v_add_co_u32_e32 v2, vcc, s6, v66
	s_mov_b32 s6, 0x9000
	s_nop 0
	v_addc_co_u32_e32 v3, vcc, 0, v67, vcc
	global_store_short_d16_hi v[2:3], v4, off offset:2048
	v_mul_f32_e32 v4, v53, v77
	v_bfe_u32 v5, v4, 16, 1
	v_add3_u32 v4, v4, v5, s37
	global_store_short_d16_hi v[2:3], v4, off offset:2112
	v_mul_f32_e32 v4, v37, v77
	v_bfe_u32 v5, v4, 16, 1
	v_add3_u32 v4, v4, v5, s37
	global_store_short_d16_hi v[2:3], v4, off offset:2176
	v_mul_f32_e32 v4, v21, v77
	v_bfe_u32 v5, v4, 16, 1
	v_add3_u32 v4, v4, v5, s37
	global_store_short_d16_hi v[2:3], v4, off offset:2240
	v_mul_f32_e32 v2, v6, v78
	v_bfe_u32 v3, v2, 16, 1
	v_add3_u32 v4, v2, v3, s37
	v_add_co_u32_e32 v2, vcc, s83, v66
	v_rcp_f32_e32 v69, v69
	s_nop 0
	v_addc_co_u32_e32 v3, vcc, 0, v67, vcc
	global_store_short_d16_hi v[2:3], v4, off offset:2048
	v_mul_f32_e32 v4, v54, v78
	v_bfe_u32 v5, v4, 16, 1
	v_add3_u32 v4, v4, v5, s37
	global_store_short_d16_hi v[2:3], v4, off offset:2112
	v_mul_f32_e32 v4, v38, v78
	v_bfe_u32 v5, v4, 16, 1
	v_add3_u32 v4, v4, v5, s37
	global_store_short_d16_hi v[2:3], v4, off offset:2176
	v_mul_f32_e32 v4, v22, v78
	v_bfe_u32 v5, v4, 16, 1
	v_add3_u32 v4, v4, v5, s37
	global_store_short_d16_hi v[2:3], v4, off offset:2240
	v_mul_f32_e32 v2, v7, v79
	v_bfe_u32 v3, v2, 16, 1
	v_add3_u32 v4, v2, v3, s37
	v_add_co_u32_e32 v2, vcc, s6, v66
; __device__ __forceinline__ unsigned f2bf(float f) { unsigned u = __builtin_bit_cast(unsigned, f); return (u + 0x7fffu + ((u >> 16) & 1u)) >> 16; }
; __device__ __forceinline__ void attn_unit(const bf16* __restrict__ Qraw, const float* __restrict__ ssq, const float* __restrict__ qn, int t0, const bf16* __restrict__ Kh, const bf16* __restrict__ Vh, bf16* __restrict__ Ob, int seq, LAS char* lds, int tid) {
;     ...
;     char* Ow = (char*)Ob + (size_t)(wid * QBLK) * DM * 2; const unsigned ooff = (unsigned)(4 * hi * DM + r32) * 2u;
; #pragma unroll
;     for (int r = 0; r < 16; ++r) {
; #pragma unroll
;         for (int d0 = 0; d0 < 4; ++d0) *(bf16*)(Ow + (((r & 3) + 8 * (r >> 2)) * DM + d0 * 32) * 2 + ooff) = (bf16)f2bf(o[d0][r] * rli[r]); }
	s_mov_b32 s6, 0xa000
	s_nop 0
	v_addc_co_u32_e32 v3, vcc, 0, v67, vcc
	global_store_short_d16_hi v[2:3], v4, off offset:2048
	v_mul_f32_e32 v4, v55, v79
	v_bfe_u32 v5, v4, 16, 1
	v_add3_u32 v4, v4, v5, s37
	global_store_short_d16_hi v[2:3], v4, off offset:2112
	v_mul_f32_e32 v4, v39, v79
	v_bfe_u32 v5, v4, 16, 1
	v_add3_u32 v4, v4, v5, s37
	global_store_short_d16_hi v[2:3], v4, off offset:2176
	v_mul_f32_e32 v4, v23, v79
	v_bfe_u32 v5, v4, 16, 1
	v_add3_u32 v4, v4, v5, s37
	global_store_short_d16_hi v[2:3], v4, off offset:2240
	v_mul_f32_e32 v2, v8, v80
	v_bfe_u32 v3, v2, 16, 1
	v_add3_u32 v4, v2, v3, s37
	v_add_co_u32_e32 v2, vcc, s6, v66
	s_mov_b32 s6, 0xb000
	s_nop 0
	v_addc_co_u32_e32 v3, vcc, 0, v67, vcc
	global_store_short_d16_hi v[2:3], v4, off offset:2048
	v_mul_f32_e32 v4, v56, v80
	v_bfe_u32 v5, v4, 16, 1
	v_add3_u32 v4, v4, v5, s37
	global_store_short_d16_hi v[2:3], v4, off offset:2112
	v_mul_f32_e32 v4, v40, v80
	v_bfe_u32 v5, v4, 16, 1
	v_add3_u32 v4, v4, v5, s37
	global_store_short_d16_hi v[2:3], v4, off offset:2176
	v_mul_f32_e32 v4, v24, v80
	v_bfe_u32 v5, v4, 16, 1
	v_add3_u32 v4, v4, v5, s37
	global_store_short_d16_hi v[2:3], v4, off offset:2240
	v_mul_f32_e32 v2, v9, v81
	v_bfe_u32 v3, v2, 16, 1
	v_add3_u32 v4, v2, v3, s37
	v_add_co_u32_e32 v2, vcc, s6, v66
	s_mov_b32 s6, 0x11000
	s_nop 0
	v_addc_co_u32_e32 v3, vcc, 0, v67, vcc
	global_store_short_d16_hi v[2:3], v4, off offset:2048
	v_mul_f32_e32 v4, v57, v81
	v_bfe_u32 v5, v4, 16, 1
	v_add3_u32 v4, v4, v5, s37
	global_store_short_d16_hi v[2:3], v4, off offset:2112
	v_mul_f32_e32 v4, v41, v81
	v_bfe_u32 v5, v4, 16, 1
	v_add3_u32 v4, v4, v5, s37
	global_store_short_d16_hi v[2:3], v4, off offset:2176
	v_mul_f32_e32 v4, v25, v81
	v_bfe_u32 v5, v4, 16, 1
	v_add3_u32 v4, v4, v5, s37
	global_store_short_d16_hi v[2:3], v4, off offset:2240
	v_mul_f32_e32 v2, v10, v1
	v_bfe_u32 v3, v2, 16, 1
	v_add3_u32 v4, v2, v3, s37
	v_add_co_u32_e32 v2, vcc, s81, v66
	s_waitcnt lgkmcnt(0)
; __device__ __forceinline__ unsigned f2bf(float f) { unsigned u = __builtin_bit_cast(unsigned, f); return (u + 0x7fffu + ((u >> 16) & 1u)) >> 16; }
; __device__ __forceinline__ void attn_unit(const bf16* __restrict__ Qraw, const float* __restrict__ ssq, const float* __restrict__ qn, int t0, const bf16* __restrict__ Kh, const bf16* __restrict__ Vh, bf16* __restrict__ Ob, int seq, LAS char* lds, int tid) {
;     ...
;     char* Ow = (char*)Ob + (size_t)(wid * QBLK) * DM * 2; const unsigned ooff = (unsigned)(4 * hi * DM + r32) * 2u;
; #pragma unroll
;     for (int r = 0; r < 16; ++r) {
; #pragma unroll
;         for (int d0 = 0; d0 < 4; ++d0) *(bf16*)(Ow + (((r & 3) + 8 * (r >> 2)) * DM + d0 * 32) * 2 + ooff) = (bf16)f2bf(o[d0][r] * rli[r]); }
;     __syncthreads();
; __device__ __forceinline__ void phase_attn(const Args& a, const Ctx& c0, int l, bool last) {
;     ...
;     for (int u = c.bid; u < nun; u += c.G) {
	v_rcp_f32_e32 v70, v70
	v_addc_co_u32_e32 v3, vcc, 0, v67, vcc
	global_store_short_d16_hi v[2:3], v4, off offset:2048
	v_mul_f32_e32 v4, v58, v1
	v_bfe_u32 v5, v4, 16, 1
	v_add3_u32 v4, v4, v5, s37
	global_store_short_d16_hi v[2:3], v4, off offset:2112
	v_mul_f32_e32 v4, v42, v1
	v_bfe_u32 v5, v4, 16, 1
	v_add3_u32 v4, v4, v5, s37
	v_mul_f32_e32 v1, v26, v1
	global_store_short_d16_hi v[2:3], v4, off offset:2176
	v_bfe_u32 v4, v1, 16, 1
	v_add3_u32 v1, v1, v4, s37
	global_store_short_d16_hi v[2:3], v1, off offset:2240
	v_mul_f32_e32 v1, v11, v82
	v_bfe_u32 v2, v1, 16, 1
	v_add3_u32 v1, v1, v2, s37
	v_add_co_u32_e32 v2, vcc, s6, v66
	s_mov_b32 s6, 0x12000
	s_nop 0
	v_addc_co_u32_e32 v3, vcc, 0, v67, vcc
	global_store_short_d16_hi v[2:3], v1, off offset:2048
	v_mul_f32_e32 v1, v59, v82
	v_bfe_u32 v4, v1, 16, 1
	v_add3_u32 v1, v1, v4, s37
	global_store_short_d16_hi v[2:3], v1, off offset:2112
	v_mul_f32_e32 v1, v43, v82
	v_bfe_u32 v4, v1, 16, 1
	v_add3_u32 v1, v1, v4, s37
	global_store_short_d16_hi v[2:3], v1, off offset:2176
	v_mul_f32_e32 v1, v27, v82
	v_bfe_u32 v4, v1, 16, 1
	v_add3_u32 v1, v1, v4, s37
	global_store_short_d16_hi v[2:3], v1, off offset:2240
	v_mul_f32_e32 v1, v12, v68
	v_bfe_u32 v2, v1, 16, 1
	v_add3_u32 v1, v1, v2, s37
	v_add_co_u32_e32 v2, vcc, s6, v66
	s_mov_b32 s6, 0x13000
	s_nop 0
	v_addc_co_u32_e32 v3, vcc, 0, v67, vcc
	global_store_short_d16_hi v[2:3], v1, off offset:2048
	v_mul_f32_e32 v1, v60, v68
	v_bfe_u32 v4, v1, 16, 1
	v_add3_u32 v1, v1, v4, s37
	global_store_short_d16_hi v[2:3], v1, off offset:2112
	v_mul_f32_e32 v1, v44, v68
	v_bfe_u32 v4, v1, 16, 1
	v_add3_u32 v1, v1, v4, s37
	global_store_short_d16_hi v[2:3], v1, off offset:2176
	v_mul_f32_e32 v1, v28, v68
	v_bfe_u32 v4, v1, 16, 1
	v_add3_u32 v1, v1, v4, s37
	global_store_short_d16_hi v[2:3], v1, off offset:2240
	v_mul_f32_e32 v1, v13, v69
	v_bfe_u32 v2, v1, 16, 1
	v_add3_u32 v1, v1, v2, s37
	v_add_co_u32_e32 v2, vcc, s6, v66
	v_rcp_f32_e32 v71, v71
	s_nop 0
	v_addc_co_u32_e32 v3, vcc, 0, v67, vcc
	global_store_short_d16_hi v[2:3], v1, off offset:2048
	v_mul_f32_e32 v1, v61, v69
	v_bfe_u32 v4, v1, 16, 1
	v_add3_u32 v1, v1, v4, s37
	global_store_short_d16_hi v[2:3], v1, off offset:2112
	v_mul_f32_e32 v1, v45, v69
	v_bfe_u32 v4, v1, 16, 1
	v_add3_u32 v1, v1, v4, s37
	global_store_short_d16_hi v[2:3], v1, off offset:2176
	v_mul_f32_e32 v1, v29, v69
	v_bfe_u32 v4, v1, 16, 1
	v_add3_u32 v1, v1, v4, s37
	global_store_short_d16_hi v[2:3], v1, off offset:2240
	v_mul_f32_e32 v1, v14, v70
	v_bfe_u32 v2, v1, 16, 1
	v_add3_u32 v1, v1, v2, s37
	v_add_co_u32_e32 v2, vcc, s82, v66
	s_mov_b32 s6, 0x19000
	s_nop 0
	v_addc_co_u32_e32 v3, vcc, 0, v67, vcc
	global_store_short_d16_hi v[2:3], v1, off offset:2048
	v_mul_f32_e32 v1, v62, v70
	v_bfe_u32 v4, v1, 16, 1
	v_add3_u32 v1, v1, v4, s37
	global_store_short_d16_hi v[2:3], v1, off offset:2112
	v_mul_f32_e32 v1, v46, v70
	v_bfe_u32 v4, v1, 16, 1
	v_add3_u32 v1, v1, v4, s37
	global_store_short_d16_hi v[2:3], v1, off offset:2176
	v_mul_f32_e32 v1, v30, v70
	v_bfe_u32 v4, v1, 16, 1
	v_add3_u32 v1, v1, v4, s37
	global_store_short_d16_hi v[2:3], v1, off offset:2240
	v_mul_f32_e32 v1, v15, v71
	v_bfe_u32 v2, v1, 16, 1
	v_add3_u32 v1, v1, v2, s37
	v_add_co_u32_e32 v2, vcc, s6, v66
	v_rcp_f32_e32 v72, v72
	s_nop 0
	v_addc_co_u32_e32 v3, vcc, 0, v67, vcc
	global_store_short_d16_hi v[2:3], v1, off offset:2048
	v_mul_f32_e32 v1, v63, v71
	v_bfe_u32 v4, v1, 16, 1
	v_add3_u32 v1, v1, v4, s37
	global_store_short_d16_hi v[2:3], v1, off offset:2112
	v_mul_f32_e32 v1, v47, v71
	v_bfe_u32 v4, v1, 16, 1
	v_add3_u32 v1, v1, v4, s37
	global_store_short_d16_hi v[2:3], v1, off offset:2176
	v_mul_f32_e32 v1, v31, v71
	v_bfe_u32 v4, v1, 16, 1
	v_add3_u32 v1, v1, v4, s37
	global_store_short_d16_hi v[2:3], v1, off offset:2240
	v_mul_f32_e32 v1, v16, v72
	v_bfe_u32 v2, v1, 16, 1
	s_mov_b32 s6, 0x1a000
	v_add3_u32 v1, v1, v2, s37
	v_add_co_u32_e32 v2, vcc, s6, v66
	v_rcp_f32_e32 v73, v73
	s_nop 0
	v_addc_co_u32_e32 v3, vcc, 0, v67, vcc
	global_store_short_d16_hi v[2:3], v1, off offset:2048
	v_mul_f32_e32 v1, v64, v72
	v_bfe_u32 v4, v1, 16, 1
	v_add3_u32 v1, v1, v4, s37
	global_store_short_d16_hi v[2:3], v1, off offset:2112
	v_mul_f32_e32 v1, v48, v72
	v_bfe_u32 v4, v1, 16, 1
	v_add3_u32 v1, v1, v4, s37
	global_store_short_d16_hi v[2:3], v1, off offset:2176
	v_mul_f32_e32 v1, v32, v72
	v_bfe_u32 v4, v1, 16, 1
	v_add3_u32 v1, v1, v4, s37
	global_store_short_d16_hi v[2:3], v1, off offset:2240
	v_mul_f32_e32 v1, v17, v73
	v_bfe_u32 v2, v1, 16, 1
	s_mov_b32 s6, 0x1b000
	v_add3_u32 v1, v1, v2, s37
	v_add_co_u32_e32 v2, vcc, s6, v66
	s_add_i32 s55, s55, s91
	s_nop 0
	v_addc_co_u32_e32 v3, vcc, 0, v67, vcc
	global_store_short_d16_hi v[2:3], v1, off offset:2048
	v_mul_f32_e32 v1, v65, v73
	v_bfe_u32 v4, v1, 16, 1
	v_add3_u32 v1, v1, v4, s37
	global_store_short_d16_hi v[2:3], v1, off offset:2112
	v_mul_f32_e32 v1, v49, v73
	v_bfe_u32 v4, v1, 16, 1
	v_add3_u32 v1, v1, v4, s37
	global_store_short_d16_hi v[2:3], v1, off offset:2176
	v_mul_f32_e32 v1, v33, v73
	v_bfe_u32 v4, v1, 16, 1
	v_add3_u32 v1, v1, v4, s37
	s_cmp_ge_i32 s55, s44
	global_store_short_d16_hi v[2:3], v1, off offset:2240
	s_waitcnt vmcnt(63) expcnt(7) lgkmcnt(15)
	s_barrier
	s_cbranch_scc1 .LBB0_1483

; __device__ __forceinline__ void phase_attn(const Args& a, const Ctx& c0, int l, bool last) {
;     ...
;     const char* HP = (const char*)WSP(const char, WS_AB); const float* CAR = WSP(const float, WS_CARRY); const bf16* GR = WSP(const bf16, WS_GR);
;     int tid2 = c0.tid; asm volatile("" : "+v"(tid2));
;     const int g4 = (tid2 & 255) * 4, rh = tid2 >> 8;
;     for (int rep = 0; rep < NREP(14); ++rep)
;     for (int it = c.bid; it < NB * NCHUNK; it += c.G) {
;         const int b = it / NCHUNK, cc = it - b * NCHUNK; if (last && cc < 4) continue;
;         const int r0 = (cc < 4 ? NL + b * CTXL + cc * 64 : b * SEQ + (cc - 4) * 64) + rh * 32;
;         const f32x4 cf = *(const f32x4*)(CAR + ((size_t)0 * NB * NCHUNK + it) * RW + g4), cb = *(const f32x4*)(CAR + ((size_t)1 * NB * NCHUNK + it) * RW + g4);
;         const char* hf = HP + ((size_t)r0 * 1024 + g4) * 4; const char* hb = hf + (size_t)NR * 1024 * 4;
.LBB0_1483:
	s_setprio 0
	v_readlane_b32 s48, v254, 35
	v_mov_b32_e32 v2, v0
	s_and_b64 vcc, exec, s[38:39]
	v_readlane_b32 s49, v254, 36
	v_readlane_b32 s50, v254, 37
	v_readlane_b32 s51, v254, 38
	v_readlane_b32 s52, v254, 39
	v_readlane_b32 s53, v254, 40
	v_readlane_b32 s54, v254, 41
	v_readlane_b32 s55, v254, 42
	v_readlane_b32 s58, v254, 45
	v_readlane_b32 s59, v254, 46
	v_readlane_b32 s60, v254, 47
	v_readlane_b32 s61, v254, 48
	v_readlane_b32 s62, v254, 49
	v_readlane_b32 s63, v254, 50
	v_readlane_b32 s56, v254, 43
	v_readlane_b32 s57, v254, 44
	s_cbranch_vccnz .LBB0_1493
	s_waitcnt lgkmcnt(0)
	v_lshlrev_b32_e32 v3, 2, v2
	v_and_b32_e32 v4, 0x3fc, v3
	v_ashrrev_i32_e32 v3, 3, v2
	s_add_u32 s10, s2, 0xd00000
	v_and_b32_e32 v11, 0xffffffe0, v3
	v_mov_b32_e32 v3, 3
	s_addc_u32 s11, s3, 0
	v_lshlrev_b32_sdwa v10, v3, v2 dst_sel:DWORD dst_unused:UNUSED_PAD src0_sel:DWORD src1_sel:BYTE_0
	v_lshlrev_b32_e32 v146, 2, v4
	s_mov_b32 s4, s90
	s_branch .LBB0_1486
